# baseline (speedup 1.0000x reference)
.Lu0_1:
	ds_read_b64_tr_b16 v[178:179], v206 offset:24576
	ds_read_b64_tr_b16 v[180:181], v206 offset:25600
	s_waitcnt lgkmcnt(9)
	v_mfma_f32_32x32x16_f16 v[98:113], v[82:85], v[154:157], v[34:49]
	v_add_f32_e32 v224, v66, v70
	v_add_f32_e32 v225, v67, v71
	v_add_f32_e32 v226, v68, v72
	v_add_f32_e32 v227, v69, v73
	v_cvt_pk_f16_f32 v158, v66, v67
	v_cvt_pk_f16_f32 v159, v68, v69
	ds_read_b64_tr_b16 v[174:175], v207 offset:24576
	ds_read_b64_tr_b16 v[176:177], v207 offset:25600
	s_waitcnt lgkmcnt(10)
	v_mfma_f32_32x32x16_f16 v[82:97], v[170:173], v[154:157], v[34:49]
	v_add_f32_e32 v224, v74, v224
	v_add_f32_e32 v225, v75, v225
	v_add_f32_e32 v226, v76, v226
	v_add_f32_e32 v227, v77, v227
	v_cvt_pk_f16_f32 v160, v70, v71
	v_cvt_pk_f16_f32 v161, v72, v73
	ds_read_b64_tr_b16 v[170:171], v206 offset:26624
	ds_read_b64_tr_b16 v[172:173], v206 offset:27648
	s_waitcnt lgkmcnt(11)
	v_mfma_f32_32x32x16_f16 v[98:113], v[166:169], v[146:149], v[98:113]
	v_add_f32_e32 v224, v78, v224
	v_add_f32_e32 v225, v79, v225
	v_add_f32_e32 v226, v80, v226
	v_add_f32_e32 v227, v81, v227
	v_cvt_pk_f16_f32 v150, v74, v75
	v_cvt_pk_f16_f32 v151, v76, v77
	ds_read_b64_tr_b16 v[74:75], v207 offset:26624
	ds_read_b64_tr_b16 v[76:77], v207 offset:27648
	s_waitcnt lgkmcnt(12)
	v_mfma_f32_32x32x16_f16 v[82:97], v[162:165], v[146:149], v[82:97]
	v_add_f32_e32 v224, v50, v224
	v_add_f32_e32 v225, v51, v225
	v_add_f32_e32 v226, v52, v226
	v_add_f32_e32 v227, v53, v227
	v_cvt_pk_f16_f32 v152, v78, v79
	v_cvt_pk_f16_f32 v153, v80, v81
	ds_read_b64_tr_b16 v[70:71], v206 offset:28672
	ds_read_b64_tr_b16 v[72:73], v206 offset:29696
	s_waitcnt lgkmcnt(13)
	v_mfma_f32_32x32x16_f16 v[98:113], v[126:129], v[138:141], v[98:113]
	v_add_f32_e32 v224, v54, v224
	v_add_f32_e32 v225, v55, v225
	v_add_f32_e32 v226, v56, v226
	v_add_f32_e32 v227, v57, v227
	v_cvt_pk_f16_f32 v142, v50, v51
	v_cvt_pk_f16_f32 v143, v52, v53
	ds_read_b64_tr_b16 v[66:67], v207 offset:28672
	ds_read_b64_tr_b16 v[68:69], v207 offset:29696
	s_waitcnt lgkmcnt(14)
	v_mfma_f32_32x32x16_f16 v[82:97], v[122:125], v[138:141], v[82:97]
	v_add_f32_e32 v224, v58, v224
	v_add_f32_e32 v225, v59, v225
	v_add_f32_e32 v226, v60, v226
	v_add_f32_e32 v227, v61, v227
	v_cvt_pk_f16_f32 v144, v54, v55
	v_cvt_pk_f16_f32 v145, v56, v57
	ds_read_b64_tr_b16 v[54:55], v206 offset:30720
	ds_read_b64_tr_b16 v[56:57], v206 offset:31744
	s_waitcnt lgkmcnt(14)
	v_mfma_f32_32x32x16_f16 v[98:113], v[118:121], v[134:137], v[98:113]
	v_add_f32_e32 v224, v62, v224
	v_add_f32_e32 v225, v63, v225
	v_add_f32_e32 v226, v64, v226
	v_add_f32_e32 v227, v65, v227
	v_cvt_pk_f16_f32 v130, v58, v59
	v_cvt_pk_f16_f32 v131, v60, v61
	ds_read_b64_tr_b16 v[50:51], v207 offset:30720
	ds_read_b64_tr_b16 v[52:53], v207 offset:31744
	v_mfma_f32_32x32x16_f16 v[82:97], v[114:117], v[134:137], v[82:97]
	s_setprio 1
	v_add_f32_e32 v224, v224, v225
	v_add_f32_e32 v226, v226, v227
	v_add_f32_e32 v60, v224, v226
	v_cvt_pk_f16_f32 v132, v62, v63
	v_cvt_pk_f16_f32 v133, v64, v65
	s_add_i32 s26, s42, s36
	s_mov_b32 m0, s26
	s_nop 0
	global_load_lds_dwordx4 v221, s[50:51]
	s_add_i32 s26, s39, s35
	s_mov_b32 m0, s26
	s_nop 0
	global_load_lds_dwordx4 v222, s[52:53]
	v_max_f32_e32 v58, v98, v99
	v_max3_f32 v59, v100, v101, v83
	v_max3_f32 v58, v58, v82, v84
	v_max3_f32 v58, v58, v85, v102
	v_max3_f32 v59, v59, v104, v105
	v_max3_f32 v58, v58, v103, v86
	v_max3_f32 v59, v59, v88, v89
	v_max3_f32 v58, v58, v87, v106
	v_max3_f32 v59, v59, v108, v109
	v_max3_f32 v58, v58, v107, v90
	v_max3_f32 v59, v59, v92, v93
	v_max3_f32 v58, v58, v91, v110
	v_max3_f32 v59, v59, v112, v113
	v_max3_f32 v58, v58, v111, v94
	v_max3_f32 v59, v59, v96, v97
	v_max3_f32 v58, v58, v95, v59
	v_add_f32_e32 v198, v183, v60
	v_cmp_lt_f32_e32 vcc, s41, v58
	s_cmp_lg_u64 vcc, 0
	s_cselect_b64 s[26:27], -1, 0
	s_cbranch_vccnz .Lu0_9

.Lu0_4:
	s_add_i32 s26, s39, 0x2000
	s_cmpk_lg_i32 s39, 0x4000
	s_cselect_b32 s43, s26, 0
	ds_read_b64_tr_b16 v[126:127], v206 offset:32768
	ds_read_b64_tr_b16 v[128:129], v206 offset:33792
	s_waitcnt lgkmcnt(9)
	v_mfma_f32_32x32x16_f16 v[66:81], v[58:61], v[154:157], v[34:49]
	v_add_f32_e32 v224, v98, v102
	v_add_f32_e32 v225, v99, v103
	v_add_f32_e32 v226, v100, v104
	v_add_f32_e32 v227, v101, v105
	v_cvt_pk_f16_f32 v158, v98, v99
	v_cvt_pk_f16_f32 v159, v100, v101
	ds_read_b64_tr_b16 v[122:123], v207 offset:32768
	ds_read_b64_tr_b16 v[124:125], v207 offset:33792
	s_waitcnt lgkmcnt(10)
	v_mfma_f32_32x32x16_f16 v[50:65], v[114:117], v[154:157], v[34:49]
	v_add_f32_e32 v224, v106, v224
	v_add_f32_e32 v225, v107, v225
	v_add_f32_e32 v226, v108, v226
	v_add_f32_e32 v227, v109, v227
	v_cvt_pk_f16_f32 v160, v102, v103
	v_cvt_pk_f16_f32 v161, v104, v105
	ds_read_b64_tr_b16 v[118:119], v206 offset:34816
	ds_read_b64_tr_b16 v[120:121], v206 offset:35840
	s_waitcnt lgkmcnt(11)
	v_mfma_f32_32x32x16_f16 v[66:81], v[182:185], v[146:149], v[66:81]
	v_add_f32_e32 v224, v110, v224
	v_add_f32_e32 v225, v111, v225
	v_add_f32_e32 v226, v112, v226
	v_add_f32_e32 v227, v113, v227
	v_cvt_pk_f16_f32 v150, v106, v107
	v_cvt_pk_f16_f32 v151, v108, v109
	ds_read_b64_tr_b16 v[114:115], v207 offset:34816
	ds_read_b64_tr_b16 v[116:117], v207 offset:35840
	s_waitcnt lgkmcnt(12)
	v_mfma_f32_32x32x16_f16 v[50:65], v[174:177], v[146:149], v[50:65]
	v_add_f32_e32 v224, v82, v224
	v_add_f32_e32 v225, v83, v225
	v_add_f32_e32 v226, v84, v226
	v_add_f32_e32 v227, v85, v227
	v_cvt_pk_f16_f32 v152, v110, v111
	v_cvt_pk_f16_f32 v153, v112, v113
	ds_read_b64_tr_b16 v[106:107], v206 offset:36864
	ds_read_b64_tr_b16 v[108:109], v206 offset:37888
	s_waitcnt lgkmcnt(13)
	v_mfma_f32_32x32x16_f16 v[66:81], v[178:181], v[138:141], v[66:81]
	v_add_f32_e32 v224, v86, v224
	v_add_f32_e32 v225, v87, v225
	v_add_f32_e32 v226, v88, v226
	v_add_f32_e32 v227, v89, v227
	v_cvt_pk_f16_f32 v142, v82, v83
	v_cvt_pk_f16_f32 v143, v84, v85
	ds_read_b64_tr_b16 v[102:103], v207 offset:36864
	ds_read_b64_tr_b16 v[104:105], v207 offset:37888
	s_waitcnt lgkmcnt(14)
	v_mfma_f32_32x32x16_f16 v[50:65], v[166:169], v[138:141], v[50:65]
	v_add_f32_e32 v224, v90, v224
	v_add_f32_e32 v225, v91, v225
	v_add_f32_e32 v226, v92, v226
	v_add_f32_e32 v227, v93, v227
	v_cvt_pk_f16_f32 v144, v86, v87
	v_cvt_pk_f16_f32 v145, v88, v89
	ds_read_b64_tr_b16 v[98:99], v206 offset:38912
	ds_read_b64_tr_b16 v[100:101], v206 offset:39936
	s_waitcnt lgkmcnt(14)
	v_mfma_f32_32x32x16_f16 v[66:81], v[170:173], v[134:137], v[66:81]
	v_add_f32_e32 v224, v94, v224
	v_add_f32_e32 v225, v95, v225
	v_add_f32_e32 v226, v96, v226
	v_add_f32_e32 v227, v97, v227
	v_cvt_pk_f16_f32 v130, v90, v91
	v_cvt_pk_f16_f32 v131, v92, v93
	ds_read_b64_tr_b16 v[86:87], v207 offset:38912
	ds_read_b64_tr_b16 v[88:89], v207 offset:39936
	v_mfma_f32_32x32x16_f16 v[50:65], v[162:165], v[134:137], v[50:65]
	s_setprio 1
	v_add_f32_e32 v224, v224, v225
	v_add_f32_e32 v226, v226, v227
	v_add_f32_e32 v84, v224, v226
	v_cvt_pk_f16_f32 v132, v94, v95
	v_cvt_pk_f16_f32 v133, v96, v97
	s_add_u32 s54, s50, 0x2000
	s_addc_u32 s55, s51, 0
	s_add_i32 s26, s39, s36
	s_mov_b32 m0, s26
	s_nop 0
	global_load_lds_dwordx4 v221, s[54:55]
	v_max_f32_e32 v82, v66, v67
	s_nop 1
	v_max3_f32 v83, v68, v69, v51
	v_max3_f32 v82, v82, v50, v52
	v_max3_f32 v82, v82, v53, v70
	v_max3_f32 v83, v83, v72, v73
	v_max3_f32 v82, v82, v71, v54
	v_max3_f32 v83, v83, v56, v57
	v_max3_f32 v82, v82, v55, v74
	v_max3_f32 v83, v83, v76, v77
	v_max3_f32 v82, v82, v75, v58
	v_max3_f32 v83, v83, v60, v61
	v_max3_f32 v82, v82, v59, v78
	v_max3_f32 v83, v83, v80, v81
	v_max3_f32 v82, v82, v79, v62
	v_max3_f32 v83, v83, v64, v65
	v_max3_f32 v82, v82, v63, v83
	v_add_f32_e32 v183, v198, v84
	s_add_u32 s54, s52, 0x2000
	s_addc_u32 s55, s53, 0
	s_add_i32 s26, s43, s35
	s_mov_b32 m0, s26
	s_nop 0
	global_load_lds_dwordx4 v222, s[54:55]
	v_cmp_lt_f32_e32 vcc, s41, v82
	s_cmp_lg_u64 vcc, 0
	s_cselect_b64 s[26:27], -1, 0
	s_cbranch_vccnz .Lu0_12

.Lu1_1:
	ds_read_b64_tr_b16 v[178:179], v206 offset:40960
	ds_read_b64_tr_b16 v[180:181], v206 offset:41984
	s_waitcnt lgkmcnt(9)
	v_mfma_f32_32x32x16_f16 v[98:113], v[82:85], v[154:157], v[34:49]
	v_add_f32_e32 v224, v66, v70
	v_add_f32_e32 v225, v67, v71
	v_add_f32_e32 v226, v68, v72
	v_add_f32_e32 v227, v69, v73
	v_cvt_pk_f16_f32 v158, v66, v67
	v_cvt_pk_f16_f32 v159, v68, v69
	ds_read_b64_tr_b16 v[174:175], v207 offset:40960
	ds_read_b64_tr_b16 v[176:177], v207 offset:41984
	s_waitcnt lgkmcnt(10)
	v_mfma_f32_32x32x16_f16 v[82:97], v[170:173], v[154:157], v[34:49]
	v_add_f32_e32 v224, v74, v224
	v_add_f32_e32 v225, v75, v225
	v_add_f32_e32 v226, v76, v226
	v_add_f32_e32 v227, v77, v227
	v_cvt_pk_f16_f32 v160, v70, v71
	v_cvt_pk_f16_f32 v161, v72, v73
	ds_read_b64_tr_b16 v[170:171], v206 offset:43008
	ds_read_b64_tr_b16 v[172:173], v206 offset:44032
	s_waitcnt lgkmcnt(11)
	v_mfma_f32_32x32x16_f16 v[98:113], v[166:169], v[146:149], v[98:113]
	v_add_f32_e32 v224, v78, v224
	v_add_f32_e32 v225, v79, v225
	v_add_f32_e32 v226, v80, v226
	v_add_f32_e32 v227, v81, v227
	v_cvt_pk_f16_f32 v150, v74, v75
	v_cvt_pk_f16_f32 v151, v76, v77
	ds_read_b64_tr_b16 v[74:75], v207 offset:43008
	ds_read_b64_tr_b16 v[76:77], v207 offset:44032
	s_waitcnt lgkmcnt(12)
	v_mfma_f32_32x32x16_f16 v[82:97], v[162:165], v[146:149], v[82:97]
	v_add_f32_e32 v224, v50, v224
	v_add_f32_e32 v225, v51, v225
	v_add_f32_e32 v226, v52, v226
	v_add_f32_e32 v227, v53, v227
	v_cvt_pk_f16_f32 v152, v78, v79
	v_cvt_pk_f16_f32 v153, v80, v81
	ds_read_b64_tr_b16 v[70:71], v206 offset:45056
	ds_read_b64_tr_b16 v[72:73], v206 offset:46080
	s_waitcnt lgkmcnt(13)
	v_mfma_f32_32x32x16_f16 v[98:113], v[126:129], v[138:141], v[98:113]
	v_add_f32_e32 v224, v54, v224
	v_add_f32_e32 v225, v55, v225
	v_add_f32_e32 v226, v56, v226
	v_add_f32_e32 v227, v57, v227
	v_cvt_pk_f16_f32 v142, v50, v51
	v_cvt_pk_f16_f32 v143, v52, v53
	ds_read_b64_tr_b16 v[66:67], v207 offset:45056
	ds_read_b64_tr_b16 v[68:69], v207 offset:46080
	s_waitcnt lgkmcnt(14)
	v_mfma_f32_32x32x16_f16 v[82:97], v[122:125], v[138:141], v[82:97]
	v_add_f32_e32 v224, v58, v224
	v_add_f32_e32 v225, v59, v225
	v_add_f32_e32 v226, v60, v226
	v_add_f32_e32 v227, v61, v227
	v_cvt_pk_f16_f32 v144, v54, v55
	v_cvt_pk_f16_f32 v145, v56, v57
	ds_read_b64_tr_b16 v[54:55], v206 offset:47104
	ds_read_b64_tr_b16 v[56:57], v206 offset:48128
	s_waitcnt lgkmcnt(14)
	v_mfma_f32_32x32x16_f16 v[98:113], v[118:121], v[134:137], v[98:113]
	v_add_f32_e32 v224, v62, v224
	v_add_f32_e32 v225, v63, v225
	v_add_f32_e32 v226, v64, v226
	v_add_f32_e32 v227, v65, v227
	v_cvt_pk_f16_f32 v130, v58, v59
	v_cvt_pk_f16_f32 v131, v60, v61
	ds_read_b64_tr_b16 v[50:51], v207 offset:47104
	ds_read_b64_tr_b16 v[52:53], v207 offset:48128
	v_mfma_f32_32x32x16_f16 v[82:97], v[114:117], v[134:137], v[82:97]
	s_setprio 1
	v_add_f32_e32 v224, v224, v225
	v_add_f32_e32 v226, v226, v227
	v_add_f32_e32 v60, v224, v226
	v_cvt_pk_f16_f32 v132, v62, v63
	v_cvt_pk_f16_f32 v133, v64, v65
	s_add_i32 s26, s42, s36
	s_mov_b32 m0, s26
	s_nop 0
	global_load_lds_dwordx4 v221, s[50:51]
	s_add_i32 s26, s39, s35
	s_mov_b32 m0, s26
	s_nop 0
	global_load_lds_dwordx4 v222, s[52:53]
	v_max_f32_e32 v58, v98, v99
	v_max3_f32 v59, v100, v101, v83
	v_max3_f32 v58, v58, v82, v84
	v_max3_f32 v58, v58, v85, v102
	v_max3_f32 v59, v59, v104, v105
	v_max3_f32 v58, v58, v103, v86
	v_max3_f32 v59, v59, v88, v89
	v_max3_f32 v58, v58, v87, v106
	v_max3_f32 v59, v59, v108, v109
	v_max3_f32 v58, v58, v107, v90
	v_max3_f32 v59, v59, v92, v93
	v_max3_f32 v58, v58, v91, v110
	v_max3_f32 v59, v59, v112, v113
	v_max3_f32 v58, v58, v111, v94
	v_max3_f32 v59, v59, v96, v97
	v_max3_f32 v58, v58, v95, v59
	v_add_f32_e32 v198, v183, v60
	v_cmp_lt_f32_e32 vcc, s41, v58
	s_cmp_lg_u64 vcc, 0
	s_cselect_b64 s[26:27], -1, 0
	s_cbranch_vccnz .Lu1_9

.Lu1_4:
	s_add_i32 s26, s39, 0x2000
	s_cmpk_lg_i32 s39, 0x4000
	s_cselect_b32 s43, s26, 0
	ds_read_b64_tr_b16 v[126:127], v206 offset:24576
	ds_read_b64_tr_b16 v[128:129], v206 offset:25600
	s_waitcnt lgkmcnt(9)
	v_mfma_f32_32x32x16_f16 v[66:81], v[58:61], v[154:157], v[34:49]
	v_add_f32_e32 v224, v98, v102
	v_add_f32_e32 v225, v99, v103
	v_add_f32_e32 v226, v100, v104
	v_add_f32_e32 v227, v101, v105
	v_cvt_pk_f16_f32 v158, v98, v99
	v_cvt_pk_f16_f32 v159, v100, v101
	ds_read_b64_tr_b16 v[122:123], v207 offset:24576
	ds_read_b64_tr_b16 v[124:125], v207 offset:25600
	s_waitcnt lgkmcnt(10)
	v_mfma_f32_32x32x16_f16 v[50:65], v[114:117], v[154:157], v[34:49]
	v_add_f32_e32 v224, v106, v224
	v_add_f32_e32 v225, v107, v225
	v_add_f32_e32 v226, v108, v226
	v_add_f32_e32 v227, v109, v227
	v_cvt_pk_f16_f32 v160, v102, v103
	v_cvt_pk_f16_f32 v161, v104, v105
	ds_read_b64_tr_b16 v[118:119], v206 offset:26624
	ds_read_b64_tr_b16 v[120:121], v206 offset:27648
	s_waitcnt lgkmcnt(11)
	v_mfma_f32_32x32x16_f16 v[66:81], v[182:185], v[146:149], v[66:81]
	v_add_f32_e32 v224, v110, v224
	v_add_f32_e32 v225, v111, v225
	v_add_f32_e32 v226, v112, v226
	v_add_f32_e32 v227, v113, v227
	v_cvt_pk_f16_f32 v150, v106, v107
	v_cvt_pk_f16_f32 v151, v108, v109
	ds_read_b64_tr_b16 v[114:115], v207 offset:26624
	ds_read_b64_tr_b16 v[116:117], v207 offset:27648
	s_waitcnt lgkmcnt(12)
	v_mfma_f32_32x32x16_f16 v[50:65], v[174:177], v[146:149], v[50:65]
	v_add_f32_e32 v224, v82, v224
	v_add_f32_e32 v225, v83, v225
	v_add_f32_e32 v226, v84, v226
	v_add_f32_e32 v227, v85, v227
	v_cvt_pk_f16_f32 v152, v110, v111
	v_cvt_pk_f16_f32 v153, v112, v113
	ds_read_b64_tr_b16 v[106:107], v206 offset:28672
	ds_read_b64_tr_b16 v[108:109], v206 offset:29696
	s_waitcnt lgkmcnt(13)
	v_mfma_f32_32x32x16_f16 v[66:81], v[178:181], v[138:141], v[66:81]
	v_add_f32_e32 v224, v86, v224
	v_add_f32_e32 v225, v87, v225
	v_add_f32_e32 v226, v88, v226
	v_add_f32_e32 v227, v89, v227
	v_cvt_pk_f16_f32 v142, v82, v83
	v_cvt_pk_f16_f32 v143, v84, v85
	ds_read_b64_tr_b16 v[102:103], v207 offset:28672
	ds_read_b64_tr_b16 v[104:105], v207 offset:29696
	s_waitcnt lgkmcnt(14)
	v_mfma_f32_32x32x16_f16 v[50:65], v[166:169], v[138:141], v[50:65]
	v_add_f32_e32 v224, v90, v224
	v_add_f32_e32 v225, v91, v225
	v_add_f32_e32 v226, v92, v226
	v_add_f32_e32 v227, v93, v227
	v_cvt_pk_f16_f32 v144, v86, v87
	v_cvt_pk_f16_f32 v145, v88, v89
	ds_read_b64_tr_b16 v[98:99], v206 offset:30720
	ds_read_b64_tr_b16 v[100:101], v206 offset:31744
	s_waitcnt lgkmcnt(14)
	v_mfma_f32_32x32x16_f16 v[66:81], v[170:173], v[134:137], v[66:81]
	v_add_f32_e32 v224, v94, v224
	v_add_f32_e32 v225, v95, v225
	v_add_f32_e32 v226, v96, v226
	v_add_f32_e32 v227, v97, v227
	v_cvt_pk_f16_f32 v130, v90, v91
	v_cvt_pk_f16_f32 v131, v92, v93
	ds_read_b64_tr_b16 v[86:87], v207 offset:30720
	ds_read_b64_tr_b16 v[88:89], v207 offset:31744
	v_mfma_f32_32x32x16_f16 v[50:65], v[162:165], v[134:137], v[50:65]
	s_setprio 1
	v_add_f32_e32 v224, v224, v225
	v_add_f32_e32 v226, v226, v227
	v_add_f32_e32 v84, v224, v226
	v_cvt_pk_f16_f32 v132, v94, v95
	v_cvt_pk_f16_f32 v133, v96, v97
	s_add_u32 s54, s50, 0x2000
	s_addc_u32 s55, s51, 0
	s_add_i32 s26, s39, s36
	s_mov_b32 m0, s26
	s_nop 0
	global_load_lds_dwordx4 v221, s[54:55]
	v_max_f32_e32 v82, v66, v67
	s_nop 1
	v_max3_f32 v83, v68, v69, v51
	v_max3_f32 v82, v82, v50, v52
	v_max3_f32 v82, v82, v53, v70
	v_max3_f32 v83, v83, v72, v73
	v_max3_f32 v82, v82, v71, v54
	v_max3_f32 v83, v83, v56, v57
	v_max3_f32 v82, v82, v55, v74
	v_max3_f32 v83, v83, v76, v77
	v_max3_f32 v82, v82, v75, v58
	v_max3_f32 v83, v83, v60, v61
	v_max3_f32 v82, v82, v59, v78
	v_max3_f32 v83, v83, v80, v81
	v_max3_f32 v82, v82, v79, v62
	v_max3_f32 v83, v83, v64, v65
	v_max3_f32 v82, v82, v63, v83
	v_add_f32_e32 v183, v198, v84
	s_add_u32 s54, s52, 0x2000
	s_addc_u32 s55, s53, 0
	s_add_i32 s26, s43, s35
	s_mov_b32 m0, s26
	s_nop 0
	global_load_lds_dwordx4 v222, s[54:55]
	v_cmp_lt_f32_e32 vcc, s41, v82
	s_cmp_lg_u64 vcc, 0
	s_cselect_b64 s[26:27], -1, 0
	s_cbranch_vccnz .Lu1_12

.Lu2_1:
	ds_read_b64_tr_b16 v[178:179], v206 offset:32768
	ds_read_b64_tr_b16 v[180:181], v206 offset:33792
	s_waitcnt lgkmcnt(9)
	v_mfma_f32_32x32x16_f16 v[98:113], v[82:85], v[154:157], v[34:49]
	v_add_f32_e32 v224, v66, v70
	v_add_f32_e32 v225, v67, v71
	v_add_f32_e32 v226, v68, v72
	v_add_f32_e32 v227, v69, v73
	v_cvt_pk_f16_f32 v158, v66, v67
	v_cvt_pk_f16_f32 v159, v68, v69
	ds_read_b64_tr_b16 v[174:175], v207 offset:32768
	ds_read_b64_tr_b16 v[176:177], v207 offset:33792
	s_waitcnt lgkmcnt(10)
	v_mfma_f32_32x32x16_f16 v[82:97], v[170:173], v[154:157], v[34:49]
	v_add_f32_e32 v224, v74, v224
	v_add_f32_e32 v225, v75, v225
	v_add_f32_e32 v226, v76, v226
	v_add_f32_e32 v227, v77, v227
	v_cvt_pk_f16_f32 v160, v70, v71
	v_cvt_pk_f16_f32 v161, v72, v73
	ds_read_b64_tr_b16 v[170:171], v206 offset:34816
	ds_read_b64_tr_b16 v[172:173], v206 offset:35840
	s_waitcnt lgkmcnt(11)
	v_mfma_f32_32x32x16_f16 v[98:113], v[166:169], v[146:149], v[98:113]
	v_add_f32_e32 v224, v78, v224
	v_add_f32_e32 v225, v79, v225
	v_add_f32_e32 v226, v80, v226
	v_add_f32_e32 v227, v81, v227
	v_cvt_pk_f16_f32 v150, v74, v75
	v_cvt_pk_f16_f32 v151, v76, v77
	ds_read_b64_tr_b16 v[74:75], v207 offset:34816
	ds_read_b64_tr_b16 v[76:77], v207 offset:35840
	s_waitcnt lgkmcnt(12)
	v_mfma_f32_32x32x16_f16 v[82:97], v[162:165], v[146:149], v[82:97]
	v_add_f32_e32 v224, v50, v224
	v_add_f32_e32 v225, v51, v225
	v_add_f32_e32 v226, v52, v226
	v_add_f32_e32 v227, v53, v227
	v_cvt_pk_f16_f32 v152, v78, v79
	v_cvt_pk_f16_f32 v153, v80, v81
	ds_read_b64_tr_b16 v[70:71], v206 offset:36864
	ds_read_b64_tr_b16 v[72:73], v206 offset:37888
	s_waitcnt lgkmcnt(13)
	v_mfma_f32_32x32x16_f16 v[98:113], v[126:129], v[138:141], v[98:113]
	v_add_f32_e32 v224, v54, v224
	v_add_f32_e32 v225, v55, v225
	v_add_f32_e32 v226, v56, v226
	v_add_f32_e32 v227, v57, v227
	v_cvt_pk_f16_f32 v142, v50, v51
	v_cvt_pk_f16_f32 v143, v52, v53
	ds_read_b64_tr_b16 v[66:67], v207 offset:36864
	ds_read_b64_tr_b16 v[68:69], v207 offset:37888
	s_waitcnt lgkmcnt(14)
	v_mfma_f32_32x32x16_f16 v[82:97], v[122:125], v[138:141], v[82:97]
	v_add_f32_e32 v224, v58, v224
	v_add_f32_e32 v225, v59, v225
	v_add_f32_e32 v226, v60, v226
	v_add_f32_e32 v227, v61, v227
	v_cvt_pk_f16_f32 v144, v54, v55
	v_cvt_pk_f16_f32 v145, v56, v57
	ds_read_b64_tr_b16 v[54:55], v206 offset:38912
	ds_read_b64_tr_b16 v[56:57], v206 offset:39936
	s_waitcnt lgkmcnt(14)
	v_mfma_f32_32x32x16_f16 v[98:113], v[118:121], v[134:137], v[98:113]
	v_add_f32_e32 v224, v62, v224
	v_add_f32_e32 v225, v63, v225
	v_add_f32_e32 v226, v64, v226
	v_add_f32_e32 v227, v65, v227
	v_cvt_pk_f16_f32 v130, v58, v59
	v_cvt_pk_f16_f32 v131, v60, v61
	ds_read_b64_tr_b16 v[50:51], v207 offset:38912
	ds_read_b64_tr_b16 v[52:53], v207 offset:39936
	v_mfma_f32_32x32x16_f16 v[82:97], v[114:117], v[134:137], v[82:97]
	s_setprio 1
	v_add_f32_e32 v224, v224, v225
	v_add_f32_e32 v226, v226, v227
	v_add_f32_e32 v60, v224, v226
	v_cvt_pk_f16_f32 v132, v62, v63
	v_cvt_pk_f16_f32 v133, v64, v65
	s_add_i32 s26, s42, s36
	s_mov_b32 m0, s26
	s_nop 0
	global_load_lds_dwordx4 v221, s[50:51]
	s_add_i32 s26, s39, s35
	s_mov_b32 m0, s26
	s_nop 0
	global_load_lds_dwordx4 v222, s[52:53]
	v_max_f32_e32 v58, v98, v99
	v_max3_f32 v59, v100, v101, v83
	v_max3_f32 v58, v58, v82, v84
	v_max3_f32 v58, v58, v85, v102
	v_max3_f32 v59, v59, v104, v105
	v_max3_f32 v58, v58, v103, v86
	v_max3_f32 v59, v59, v88, v89
	v_max3_f32 v58, v58, v87, v106
	v_max3_f32 v59, v59, v108, v109
	v_max3_f32 v58, v58, v107, v90
	v_max3_f32 v59, v59, v92, v93
	v_max3_f32 v58, v58, v91, v110
	v_max3_f32 v59, v59, v112, v113
	v_max3_f32 v58, v58, v111, v94
	v_max3_f32 v59, v59, v96, v97
	v_max3_f32 v58, v58, v95, v59
	v_add_f32_e32 v198, v183, v60
	v_cmp_lt_f32_e32 vcc, s41, v58
	s_cmp_lg_u64 vcc, 0
	s_cselect_b64 s[26:27], -1, 0
	s_cbranch_vccnz .Lu2_9

.Lu2_4:
	s_add_i32 s26, s39, 0x2000
	s_cmpk_lg_i32 s39, 0x4000
	s_cselect_b32 s43, s26, 0
	ds_read_b64_tr_b16 v[126:127], v206 offset:40960
	ds_read_b64_tr_b16 v[128:129], v206 offset:41984
	s_waitcnt lgkmcnt(9)
	v_mfma_f32_32x32x16_f16 v[66:81], v[58:61], v[154:157], v[34:49]
	v_add_f32_e32 v224, v98, v102
	v_add_f32_e32 v225, v99, v103
	v_add_f32_e32 v226, v100, v104
	v_add_f32_e32 v227, v101, v105
	v_cvt_pk_f16_f32 v158, v98, v99
	v_cvt_pk_f16_f32 v159, v100, v101
	ds_read_b64_tr_b16 v[122:123], v207 offset:40960
	ds_read_b64_tr_b16 v[124:125], v207 offset:41984
	s_waitcnt lgkmcnt(10)
	v_mfma_f32_32x32x16_f16 v[50:65], v[114:117], v[154:157], v[34:49]
	v_add_f32_e32 v224, v106, v224
	v_add_f32_e32 v225, v107, v225
	v_add_f32_e32 v226, v108, v226
	v_add_f32_e32 v227, v109, v227
	v_cvt_pk_f16_f32 v160, v102, v103
	v_cvt_pk_f16_f32 v161, v104, v105
	ds_read_b64_tr_b16 v[118:119], v206 offset:43008
	ds_read_b64_tr_b16 v[120:121], v206 offset:44032
	s_waitcnt lgkmcnt(11)
	v_mfma_f32_32x32x16_f16 v[66:81], v[182:185], v[146:149], v[66:81]
	v_add_f32_e32 v224, v110, v224
	v_add_f32_e32 v225, v111, v225
	v_add_f32_e32 v226, v112, v226
	v_add_f32_e32 v227, v113, v227
	v_cvt_pk_f16_f32 v150, v106, v107
	v_cvt_pk_f16_f32 v151, v108, v109
	ds_read_b64_tr_b16 v[114:115], v207 offset:43008
	ds_read_b64_tr_b16 v[116:117], v207 offset:44032
	s_waitcnt lgkmcnt(12)
	v_mfma_f32_32x32x16_f16 v[50:65], v[174:177], v[146:149], v[50:65]
	v_add_f32_e32 v224, v82, v224
	v_add_f32_e32 v225, v83, v225
	v_add_f32_e32 v226, v84, v226
	v_add_f32_e32 v227, v85, v227
	v_cvt_pk_f16_f32 v152, v110, v111
	v_cvt_pk_f16_f32 v153, v112, v113
	ds_read_b64_tr_b16 v[106:107], v206 offset:45056
	ds_read_b64_tr_b16 v[108:109], v206 offset:46080
	s_waitcnt lgkmcnt(13)
	v_mfma_f32_32x32x16_f16 v[66:81], v[178:181], v[138:141], v[66:81]
	v_add_f32_e32 v224, v86, v224
	v_add_f32_e32 v225, v87, v225
	v_add_f32_e32 v226, v88, v226
	v_add_f32_e32 v227, v89, v227
	v_cvt_pk_f16_f32 v142, v82, v83
	v_cvt_pk_f16_f32 v143, v84, v85
	ds_read_b64_tr_b16 v[102:103], v207 offset:45056
	ds_read_b64_tr_b16 v[104:105], v207 offset:46080
	s_waitcnt lgkmcnt(14)
	v_mfma_f32_32x32x16_f16 v[50:65], v[166:169], v[138:141], v[50:65]
	v_add_f32_e32 v224, v90, v224
	v_add_f32_e32 v225, v91, v225
	v_add_f32_e32 v226, v92, v226
	v_add_f32_e32 v227, v93, v227
	v_cvt_pk_f16_f32 v144, v86, v87
	v_cvt_pk_f16_f32 v145, v88, v89
	ds_read_b64_tr_b16 v[98:99], v206 offset:47104
	ds_read_b64_tr_b16 v[100:101], v206 offset:48128
	s_waitcnt lgkmcnt(14)
	v_mfma_f32_32x32x16_f16 v[66:81], v[170:173], v[134:137], v[66:81]
	v_add_f32_e32 v224, v94, v224
	v_add_f32_e32 v225, v95, v225
	v_add_f32_e32 v226, v96, v226
	v_add_f32_e32 v227, v97, v227
	v_cvt_pk_f16_f32 v130, v90, v91
	v_cvt_pk_f16_f32 v131, v92, v93
	ds_read_b64_tr_b16 v[86:87], v207 offset:47104
	ds_read_b64_tr_b16 v[88:89], v207 offset:48128
	v_mfma_f32_32x32x16_f16 v[50:65], v[162:165], v[134:137], v[50:65]
	s_setprio 1
	v_add_f32_e32 v224, v224, v225
	v_add_f32_e32 v226, v226, v227
	v_add_f32_e32 v84, v224, v226
	v_cvt_pk_f16_f32 v132, v94, v95
	v_cvt_pk_f16_f32 v133, v96, v97
	s_add_u32 s54, s50, 0x2000
	s_addc_u32 s55, s51, 0
	s_add_i32 s26, s39, s36
	s_mov_b32 m0, s26
	s_nop 0
	global_load_lds_dwordx4 v221, s[54:55]
	v_max_f32_e32 v82, v66, v67
	s_nop 1
	v_max3_f32 v83, v68, v69, v51
	v_max3_f32 v82, v82, v50, v52
	v_max3_f32 v82, v82, v53, v70
	v_max3_f32 v83, v83, v72, v73
	v_max3_f32 v82, v82, v71, v54
	v_max3_f32 v83, v83, v56, v57
	v_max3_f32 v82, v82, v55, v74
	v_max3_f32 v83, v83, v76, v77
	v_max3_f32 v82, v82, v75, v58
	v_max3_f32 v83, v83, v60, v61
	v_max3_f32 v82, v82, v59, v78
	v_max3_f32 v83, v83, v80, v81
	v_max3_f32 v82, v82, v79, v62
	v_max3_f32 v83, v83, v64, v65
	v_max3_f32 v82, v82, v63, v83
	v_add_f32_e32 v183, v198, v84
	s_add_u32 s54, s52, 0x2000
	s_addc_u32 s55, s53, 0
	s_add_i32 s26, s43, s35
	s_mov_b32 m0, s26
	s_nop 0
	global_load_lds_dwordx4 v222, s[54:55]
	v_cmp_lt_f32_e32 vcc, s41, v82
	s_cmp_lg_u64 vcc, 0
	s_cselect_b64 s[26:27], -1, 0
	s_cbranch_vccnz .Lu2_12
